# deferred PEER-table conversion routines of the output / query GEMM phases moved in front of the tile-less workgroups' tiles (their epilogue bursts no longer coincide with the three-tile workgroups')
# baseline (speedup 1.0000x reference)
.LBB0_663:
	s_andn2_b64 vcc, exec, s[6:7]
	s_cbranch_vccnz .LBB0_760
	v_readlane_b32 s4, v255, 34
	s_nop 0
	s_cmp_lg_u32 s4, 0
	s_cbranch_scc1 .Ldfb1_done
	s_cmp_gt_u32 s82, 32
	s_cselect_b32 s11, 32, 0
	s_cmp_lt_u32 s2, s11
	s_cbranch_scc1 .Ldfb1_done
	s_sub_u32 s10, s82, s11
	s_lshl_b32 s10, s10, 3
	s_sub_u32 s4, s2, s11
	s_lshl_b32 s4, s4, 3
	v_readfirstlane_b32 s11, v0
	s_lshr_b32 s11, s11, 6
	s_add_u32 s4, s4, s11
	s_add_u32 s4, s4, 0x5208
	s_cmp_ge_u32 s4, 0x8000
	s_cbranch_scc1 .Ldfb1_done
	v_readlane_b32 s6, v252, 4
	v_readlane_b32 s7, v252, 5
	s_nop 0
	s_sub_u32 s6, s6, 0x38
	s_subb_u32 s7, s7, 0
	s_load_dwordx2 s[8:9], s[6:7], 0x0
	s_load_dwordx2 s[6:7], s[6:7], 0x20
	v_and_b32_e32 v6, 63, v0
	v_lshlrev_b32_e32 v7, 4, v6
	v_lshrrev_b32_e32 v56, 5, v6
	v_and_b32_e32 v57, 31, v6
	v_lshlrev_b32_e32 v56, 21, v56
	v_lshl_add_u32 v56, v57, 2, v56
	v_add_u32_e32 v56, 0xaa00000, v56
	s_mov_b64 exec, -1
	s_waitcnt lgkmcnt(0)
	s_lshl_b32 s11, s4, 13
	v_add_u32_e32 v40, s11, v7
	v_add_u32_e32 v41, 0x1000, v40
	global_load_dwordx4 v[8:11], v40, s[8:9] nt
	global_load_dwordx4 v[12:15], v40, s[8:9] offset:1024 nt
	global_load_dwordx4 v[16:19], v40, s[8:9] offset:2048 nt
	global_load_dwordx4 v[20:23], v40, s[8:9] offset:3072 nt
	global_load_dwordx4 v[24:27], v41, s[8:9] nt
	global_load_dwordx4 v[28:31], v41, s[8:9] offset:1024 nt
	global_load_dwordx4 v[32:35], v41, s[8:9] offset:2048 nt
	global_load_dwordx4 v[36:39], v41, s[8:9] offset:3072 nt

.Ldfb2_done:
	v_readlane_b32 s10, v255, 34
	v_readlane_b32 s11, v255, 35
	s_mov_b32 s11, s85
	s_lshl_b64 s[6:7], s[10:11], 22
	v_readlane_b32 s4, v254, 8
	s_add_u32 s84, s4, s6
	v_readlane_b32 s4, v254, 9
	s_addc_u32 s6, s4, s7
	s_lshr_b32 s97, s96, 8
	s_lshr_b32 s12, s96, 5
	s_mul_i32 s7, s10, 0x3c000
	v_readlane_b32 s4, v252, 40
	s_add_u32 s7, s4, s7
	v_readlane_b32 s4, v252, 41
	s_addc_u32 s8, s4, 0
	s_add_u32 s53, s7, 0x4000
	v_readlane_b32 s56, v252, 6
	s_addc_u32 s55, s8, 0
	s_mul_i32 s7, s10, 0xc000
	v_readlane_b32 s66, v252, 16
	s_mov_b32 s4, s10
	v_readlane_b32 s67, v252, 17
	s_add_u32 s7, s66, s7
	v_writelane_b32 v255, s4, 34
	s_addc_u32 s9, s67, 0
	s_mov_b32 s8, s12
	v_writelane_b32 v255, s5, 35
	s_add_u32 s4, s7, 0x4000
	s_addc_u32 s5, s9, 0
	v_writelane_b32 v255, s4, 43
	s_mov_b64 s[10:11], -1
	v_readlane_b32 s57, v252, 7
	v_writelane_b32 v255, s5, 44
	v_readlane_b32 s58, v252, 8
	v_readlane_b32 s4, v255, 39
	v_readlane_b32 s5, v255, 40
	s_and_b64 vcc, exec, s[4:5]
	v_readlane_b32 s59, v252, 9
	v_readlane_b32 s60, v252, 10
	v_readlane_b32 s61, v252, 11
	v_readlane_b32 s62, v252, 12
	v_readlane_b32 s63, v252, 13
	v_readlane_b32 s64, v252, 14
	v_readlane_b32 s65, v252, 15
	v_readlane_b32 s68, v252, 18
	v_readlane_b32 s69, v252, 19
	v_readlane_b32 s70, v252, 20
	v_readlane_b32 s71, v252, 21
	s_cbranch_vccz .LBB0_685
	v_mov_b32_e32 v3, v0
	v_mov_b32_e32 v182, 0x7f7f7f7f
	v_readfirstlane_b32 s7, v3
	s_ashr_i32 s10, s7, 6
	s_ashr_i32 s12, s7, 8
	v_and_b32_e32 v5, 15, v3
	v_bfe_u32 v175, v3, 4, 2
	s_waitcnt vmcnt(0)
	v_lshlrev_b32_e32 v7, 2, v3
	s_lshl_b32 s13, s10, 5
	v_lshlrev_b32_e32 v2, 4, v175
	s_lshl_b32 s11, s12, 13
	v_lshlrev_b32_e32 v6, 6, v5
	v_and_b32_e32 v7, 32, v7
	s_and_b32 s56, s13, 0x60
	v_bitop3_b32 v2, v6, v7, v2 bitop3:0x36
	s_lshl_b32 s13, s56, 7
	s_add_i32 s11, s11, 0
	v_add_u32_e32 v183, s11, v2
	s_add_i32 s11, s13, 0
	s_add_i32 s11, s11, 0x10000
	v_add_u32_e32 v184, s11, v2
	s_cmp_ge_i32 s2, s8
	s_cbranch_scc1 .LBB0_684
	s_waitcnt lgkmcnt(0)
	v_lshlrev_b32_e32 v10, 4, v3
	v_add_u32_e32 v2, 0x2000, v10
	v_ashrrev_i32_e32 v6, 31, v2
	v_lshrrev_b32_e32 v6, 22, v6
	v_add_u32_e32 v6, v2, v6
	v_ashrrev_i32_e32 v6, 10, v6
	v_lshlrev_b32_e32 v7, 5, v6
	v_and_b32_e32 v9, 32, v7
	v_mul_i32_i24_e32 v7, 0x400, v6
	v_sub_u32_e32 v2, v2, v7
	v_lshrrev_b32_e32 v7, 4, v2
	v_bitop3_b32 v2, v7, v2, 32 bitop3:0x6c
	v_ashrrev_i32_e32 v7, 31, v2
	v_lshrrev_b32_e32 v7, 26, v7
	v_add_u32_e32 v8, v2, v7
	v_ashrrev_i32_e32 v7, 6, v8
	v_and_b32_e32 v8, 0xc0, v8
	v_sub_u32_e32 v2, v2, v8
	v_ashrrev_i16_sdwa v2, v201, sext(v2) dst_sel:DWORD dst_unused:UNUSED_PAD src0_sel:DWORD src1_sel:BYTE_0
	v_bfe_i32 v8, v2, 0, 16
	v_add_u32_e32 v2, v9, v8
	v_lshlrev_b32_e32 v9, 3, v6
	v_and_b32_e32 v9, 0x1ffff0, v9
	v_add_lshl_u32 v9, v7, v9, 11
	v_lshl_add_u32 v2, v2, 1, v9
	v_ashrrev_i32_e32 v9, 31, v3
	v_lshrrev_b32_e32 v9, 26, v9
	v_add_u32_e32 v9, v3, v9
	v_bfe_i32 v3, v3, 27, 1
	v_lshrrev_b32_e32 v3, 22, v3
	v_add_u32_e32 v3, v10, v3
	v_and_b32_e32 v3, 0xfffffc00, v3
	v_sub_u32_e32 v3, v10, v3
	v_lshrrev_b32_e32 v10, 4, v3
	v_readlane_b32 s4, v254, 38
	s_lshl_b32 s13, s10, 10
	v_bitop3_b32 v3, v10, v3, 32 bitop3:0x6c
	s_or_b32 s10, s97, s4
	v_readlane_b32 s4, v254, 37
	v_ashrrev_i32_e32 v9, 6, v9
	v_ashrrev_i32_e32 v10, 31, v3
	s_mul_i32 s10, s10, s4
	v_readlane_b32 s4, v252, 53
	v_lshlrev_b32_e32 v11, 5, v9
	v_lshrrev_b32_e32 v10, 26, v10
	s_add_i32 s10, s10, s4
	v_and_b32_e32 v12, 32, v11
	v_add_u32_e32 v11, v3, v10
	s_ashr_i32 s11, s10, 31
	v_ashrrev_i32_e32 v10, 6, v11
	v_and_b32_e32 v11, 0xc0, v11
	s_lshr_b32 s11, s11, 27
	v_sub_u32_e32 v3, v3, v11
	s_add_i32 s11, s10, s11
	v_ashrrev_i16_sdwa v3, v201, sext(v3) dst_sel:DWORD dst_unused:UNUSED_PAD src0_sel:DWORD src1_sel:BYTE_0
	s_ashr_i32 s14, s11, 5
	v_bfe_i32 v11, v3, 0, 16
	s_lshl_b32 s14, s14, 2
	v_add_u32_e32 v3, v12, v11
	v_lshlrev_b32_e32 v12, 3, v9
	s_sub_i32 s15, s97, s14
	v_and_b32_e32 v12, 0x1ffff0, v12
	s_min_i32 s15, s15, 4
	v_add_lshl_u32 v12, v10, v12, 11
	s_abs_i32 s17, s15
	v_lshl_add_u32 v166, v3, 1, v12
	v_cvt_f32_u32_e32 v3, s17
	s_sub_i32 s18, 0, s17
	s_andn2_b32 s11, s11, 31
	s_sub_i32 s10, s10, s11
	v_rcp_iflag_f32_e32 v3, v3
	s_abs_i32 s16, s10
	s_xor_b32 s11, s10, s15
	s_ashr_i32 s11, s11, 31
	v_mul_f32_e32 v3, 0x4f7ffffe, v3
	v_cvt_u32_f32_e32 v3, v3
	s_nop 0
	v_readfirstlane_b32 s19, v3
	s_mul_i32 s18, s18, s19
	s_mul_hi_u32 s18, s19, s18
	s_add_i32 s19, s19, s18
	s_mul_hi_u32 s18, s16, s19
	s_mul_i32 s19, s18, s17
	s_sub_i32 s16, s16, s19
	s_add_i32 s19, s18, 1
	s_sub_i32 s38, s16, s17
	s_cmp_ge_u32 s16, s17
	s_cselect_b32 s18, s19, s18
	s_cselect_b32 s16, s38, s16
	s_add_i32 s19, s18, 1
	s_cmp_ge_u32 s16, s17
	s_cselect_b32 s16, s19, s18
	s_xor_b32 s16, s16, s11
	s_sub_i32 s42, s16, s11
	s_mul_i32 s11, s42, s15
	s_sub_i32 s10, s10, s11
	s_add_i32 s44, s14, s10
	s_ashr_i32 s45, s44, 31
	s_ashr_i32 s43, s42, 31
	s_lshl_b64 s[10:11], s[44:45], 19
	s_lshl_b64 s[14:15], s[42:43], 19
	s_add_u32 s48, s84, s14
	s_addc_u32 s49, s6, s15
	s_add_i32 s45, s13, 0
	s_add_i32 s57, s45, 0x10000
	s_add_i32 s58, s45, 0x12000
	s_mov_b32 m0, s57
	s_add_u32 s14, s48, 0x40000
	global_load_lds_dwordx4 v166, s[48:49]
	s_mov_b32 m0, s58
	s_addc_u32 s15, s49, 0
	s_add_i32 s59, s45, 0x14000
	s_add_i32 s60, s45, 0x16000
	global_load_lds_dwordx4 v2, s[48:49]
	s_mov_b32 m0, s59
	s_add_u32 s46, s74, s10
	global_load_lds_dwordx4 v166, s[14:15]
	s_mov_b32 m0, s60
	s_addc_u32 s47, s75, s11
	s_add_i32 s61, s45, 0x2000
	global_load_lds_dwordx4 v2, s[14:15]
	s_mov_b32 m0, s45
	s_add_u32 s10, s46, 0x40000
	global_load_lds_dwordx4 v166, s[46:47]
	s_mov_b32 m0, s61
	s_addc_u32 s11, s47, 0
	s_add_i32 s62, s45, 0x4000
	global_load_lds_dwordx4 v2, s[46:47]
	s_mov_b32 m0, s62
	s_add_i32 s63, s45, 0x6000
	global_load_lds_dwordx4 v166, s[10:11]
	s_mov_b32 m0, s63
	s_cmp_eq_u32 s12, 1
	global_load_lds_dwordx4 v2, s[10:11]
	s_cselect_b64 s[10:11], -1, 0
	s_cmp_lg_u32 s12, 1
	s_cbranch_scc1 .LBB0_668
	s_barrier

.LBB0_709:
	v_readlane_b32 s4, v255, 36
	v_readlane_b32 s8, v252, 0
	s_add_i32 s5, s4, 8
	v_readlane_b32 s9, v252, 1
	s_cmp_ge_i32 s5, s9
	v_readlane_b32 s10, v252, 2
	v_readlane_b32 s11, v252, 3
	s_cbranch_scc1 .LBB0_721
	v_readlane_b32 s8, v252, 0
	v_readlane_b32 s9, v252, 1
	v_readlane_b32 s10, v252, 2
	v_readlane_b32 s11, v252, 3

.LBB0_836:
	s_andn2_b64 vcc, exec, s[6:7]
	s_cbranch_vccnz .LBB0_906
	v_readlane_b32 s4, v255, 34
	s_nop 0
	s_cmp_lg_u32 s4, 0
	s_cbranch_scc1 .Ldfc_done
	s_cmp_gt_u32 s82, 32
	s_cselect_b32 s11, 32, 0
	s_cmp_lt_u32 s2, s11
	s_cbranch_scc1 .Ldfc_done
	s_sub_u32 s10, s82, s11
	s_lshl_b32 s10, s10, 3
	s_sub_u32 s4, s2, s11
	s_lshl_b32 s4, s4, 3
	v_readfirstlane_b32 s11, v0
	s_lshr_b32 s11, s11, 6
	s_add_u32 s4, s4, s11
	s_add_u32 s4, s4, 0x4bb8
	s_cmp_ge_u32 s4, 0x8000
	s_cbranch_scc1 .Ldfc_done
	v_readlane_b32 s6, v252, 4
	v_readlane_b32 s7, v252, 5
	s_nop 0
	s_sub_u32 s6, s6, 0x38
	s_subb_u32 s7, s7, 0
	s_load_dwordx2 s[8:9], s[6:7], 0x8
	s_load_dwordx2 s[6:7], s[6:7], 0x20
	v_and_b32_e32 v6, 63, v0
	v_lshlrev_b32_e32 v7, 4, v6
	v_lshrrev_b32_e32 v56, 5, v6
	v_and_b32_e32 v57, 31, v6
	v_lshlrev_b32_e32 v56, 21, v56
	v_lshl_add_u32 v56, v57, 2, v56
	v_add_u32_e32 v56, 0xea00000, v56
	s_mov_b64 exec, -1
	s_waitcnt lgkmcnt(0)
	s_lshl_b32 s11, s4, 13
	v_add_u32_e32 v40, s11, v7
	v_add_u32_e32 v41, 0x1000, v40
	global_load_dwordx4 v[8:11], v40, s[8:9] nt
	global_load_dwordx4 v[12:15], v40, s[8:9] offset:1024 nt
	global_load_dwordx4 v[16:19], v40, s[8:9] offset:2048 nt
	global_load_dwordx4 v[20:23], v40, s[8:9] offset:3072 nt
	global_load_dwordx4 v[24:27], v41, s[8:9] nt
	global_load_dwordx4 v[28:31], v41, s[8:9] offset:1024 nt
	global_load_dwordx4 v[32:35], v41, s[8:9] offset:2048 nt
	global_load_dwordx4 v[36:39], v41, s[8:9] offset:3072 nt

.Ldfc_done:
	v_mov_b32_e32 v3, v0
	s_lshr_b32 s84, s96, 5
	v_readfirstlane_b32 s8, v3
	s_ashr_i32 s6, s8, 6
	v_lshrrev_b32_e32 v2, 1, v3
	s_lshl_b32 s5, s6, 5
	s_waitcnt vmcnt(0)
	v_and_b32_e32 v6, 24, v2
	s_ashr_i32 s9, s8, 8
	s_and_b32 s10, s5, 0x60
	v_and_b32_e32 v7, 15, v3
	v_lshlrev_b32_e32 v2, 1, v6
	v_lshlrev_b32_e32 v5, 2, v3
	s_lshl_b32 s7, s9, 13
	s_lshl_b32 s11, s10, 7
	v_lshl_or_b32 v2, v7, 6, v2
	v_and_b32_e32 v5, 32, v5
	s_add_i32 s5, 0, 0x10000
	v_bitop3_b32 v8, v2, s7, v5 bitop3:0xde
	v_bitop3_b32 v5, v2, s11, v5 bitop3:0xde
	v_mov_b32_e32 v2, 0x7f7f7f7f
	v_add_u32_e32 v146, 0, v8
	v_add_u32_e32 v147, s5, v5
	s_cmp_ge_i32 s2, s84
	v_mov_b32_e32 v2, v146
	v_mov_b32_e32 v8, v147
	s_cbranch_scc1 .LBB0_856
	s_waitcnt lgkmcnt(0)
	v_lshlrev_b32_e32 v11, 4, v3
	v_add_u32_e32 v2, 0x2000, v11
	v_ashrrev_i32_e32 v8, 31, v2
	v_lshrrev_b32_e32 v8, 22, v8
	v_add_u32_e32 v8, v2, v8
	v_ashrrev_i32_e32 v8, 10, v8
	v_mul_i32_i24_e32 v9, 0x400, v8
	v_sub_u32_e32 v2, v2, v9
	v_lshrrev_b32_e32 v9, 4, v2
	v_bitop3_b32 v2, v9, v2, 32 bitop3:0x6c
	v_ashrrev_i32_e32 v9, 31, v2
	v_lshrrev_b32_e32 v9, 26, v9
	v_readlane_b32 s12, v255, 34
	v_add_u32_e32 v10, v2, v9
	v_lshlrev_b32_e32 v12, 3, v8
	s_lshl_b32 s7, s12, 23
	v_readlane_b32 s4, v254, 10
	v_ashrrev_i32_e32 v9, 6, v10
	v_and_b32_e32 v12, -16, v12
	s_add_u32 s48, s4, s7
	v_readlane_b32 s4, v254, 11
	v_add_u32_e32 v12, v9, v12
	s_addc_u32 s49, s4, 0
	v_and_b32_e32 v13, 3, v9
	s_mov_b32 s4, 0xfffe0
	v_lshrrev_b32_e32 v14, 2, v12
	v_lshlrev_b32_e32 v15, 1, v12
	v_and_b32_e32 v10, 0xc0, v10
	v_and_or_b32 v13, v12, s4, v13
	v_and_b32_e32 v14, 4, v14
	v_and_b32_e32 v15, 24, v15
	v_sub_u32_e32 v2, v2, v10
	v_or3_b32 v13, v13, v14, v15
	v_lshlrev_b32_e32 v14, 5, v8
	v_ashrrev_i16_sdwa v2, v201, sext(v2) dst_sel:DWORD dst_unused:UNUSED_PAD src0_sel:DWORD src1_sel:BYTE_0
	v_and_b32_e32 v14, 32, v14
	v_bfe_i32 v10, v2, 0, 16
	v_add_lshl_u32 v14, v14, v10, 1
	v_lshl_add_u32 v134, v12, 12, v14
	v_bfe_i32 v12, v3, 27, 1
	v_lshrrev_b32_e32 v12, 22, v12
	v_add_u32_e32 v12, v11, v12
	v_and_b32_e32 v12, 0xfffffc00, v12
	v_sub_u32_e32 v11, v11, v12
	v_lshrrev_b32_e32 v12, 4, v11
	v_lshl_add_u32 v2, v13, 12, v14
	v_bitop3_b32 v13, v12, v11, 32 bitop3:0x6c
	v_ashrrev_i32_e32 v12, 31, v3
	v_lshrrev_b32_e32 v12, 26, v12
	v_ashrrev_i32_e32 v11, 31, v13
	v_add_u32_e32 v3, v3, v12
	v_lshrrev_b32_e32 v11, 26, v11
	v_ashrrev_i32_e32 v12, 6, v3
	v_add_u32_e32 v14, v13, v11
	v_lshlrev_b32_e32 v3, 3, v12
	v_ashrrev_i32_e32 v11, 6, v14
	v_and_b32_e32 v3, -16, v3
	v_add_u32_e32 v3, v11, v3
	v_and_b32_e32 v15, 3, v11
	s_lshr_b32 s50, s96, 8
	v_and_or_b32 v15, v3, s4, v15
	v_readlane_b32 s4, v254, 38
	s_lshl_b32 s51, s6, 10
	s_or_b32 s6, s50, s4
	v_readlane_b32 s4, v254, 37
	s_mul_i32 s6, s6, s4
	v_readlane_b32 s4, v252, 53
	s_add_i32 s6, s6, s4
	s_ashr_i32 s7, s6, 31
	s_lshr_b32 s7, s7, 27
	s_add_i32 s7, s6, s7
	s_ashr_i32 s11, s7, 5
	s_lshl_b32 s11, s11, 2
	s_sub_i32 s12, s50, s11
	v_readlane_b32 s13, v255, 35
	s_min_i32 s12, s12, 4
	v_lshrrev_b32_e32 v16, 2, v3
	v_lshlrev_b32_e32 v17, 1, v3
	v_and_b32_e32 v14, 0xc0, v14
	s_abs_i32 s13, s12
	v_and_b32_e32 v16, 4, v16
	v_and_b32_e32 v17, 24, v17
	v_sub_u32_e32 v13, v13, v14
	v_cvt_f32_u32_e32 v14, s13
	v_or3_b32 v15, v15, v16, v17
	v_lshlrev_b32_e32 v16, 5, v12
	v_ashrrev_i16_sdwa v13, v201, sext(v13) dst_sel:DWORD dst_unused:UNUSED_PAD src0_sel:DWORD src1_sel:BYTE_0
	v_and_b32_e32 v16, 32, v16
	v_bfe_i32 v13, v13, 0, 16
	v_add_lshl_u32 v16, v16, v13, 1
	v_lshl_add_u32 v138, v3, 12, v16
	v_rcp_iflag_f32_e32 v3, v14
	s_sub_i32 s15, 0, s13
	s_andn2_b32 s7, s7, 31
	s_sub_i32 s6, s6, s7
	v_mul_f32_e32 v3, 0x4f7ffffe, v3
	v_cvt_u32_f32_e32 v3, v3
	s_abs_i32 s14, s6
	s_xor_b32 s7, s6, s12
	s_ashr_i32 s7, s7, 31
	v_readfirstlane_b32 s16, v3
	s_mul_i32 s15, s15, s16
	s_mul_hi_u32 s15, s16, s15
	s_add_i32 s16, s16, s15
	s_mul_hi_u32 s15, s14, s16
	s_mul_i32 s16, s15, s13
	s_sub_i32 s14, s14, s16
	s_add_i32 s16, s15, 1
	s_sub_i32 s17, s14, s13
	s_cmp_ge_u32 s14, s13
	s_cselect_b32 s15, s16, s15
	s_cselect_b32 s14, s17, s14
	s_add_i32 s16, s15, 1
	s_cmp_ge_u32 s14, s13
	s_cselect_b32 s13, s16, s15
	s_xor_b32 s13, s13, s7
	s_sub_i32 s38, s13, s7
	s_mul_i32 s7, s38, s12
	s_sub_i32 s6, s6, s7
	s_add_i32 s40, s11, s6
	s_ashr_i32 s41, s40, 31
	s_ashr_i32 s39, s38, 31
	s_lshl_b64 s[6:7], s[40:41], 20
	s_lshl_b64 s[12:13], s[38:39], 20
	s_add_u32 s44, s48, s12
	s_addc_u32 s45, s49, s13
	s_add_i32 s39, s51, 0
	v_lshl_add_u32 v136, v15, 12, v16
	s_add_i32 m0, s39, 0x10000
	s_nop 0
	global_load_lds_dwordx4 v136, s[44:45]
	s_add_i32 m0, s39, 0x12000
	s_add_u32 s12, s44, 0x80000
	global_load_lds_dwordx4 v2, s[44:45]
	s_addc_u32 s13, s45, 0
	s_add_i32 m0, s39, 0x14000
	s_nop 0
	global_load_lds_dwordx4 v136, s[12:13]
	s_add_i32 m0, s39, 0x16000
	s_add_u32 s42, s74, s6
	s_addc_u32 s43, s75, s7
	s_add_i32 s41, s39, 0x2000
	global_load_lds_dwordx4 v2, s[12:13]
	s_mov_b32 m0, s39
	s_add_u32 s6, s42, 0x80000
	global_load_lds_dwordx4 v138, s[42:43]
	s_mov_b32 m0, s41
	s_addc_u32 s7, s43, 0
	s_add_i32 s52, s39, 0x4000
	global_load_lds_dwordx4 v134, s[42:43]
	s_mov_b32 m0, s52
	s_add_i32 s53, s39, 0x6000
	global_load_lds_dwordx4 v138, s[6:7]
	s_mov_b32 m0, s53
	s_cmp_eq_u32 s9, 1
	global_load_lds_dwordx4 v134, s[6:7]
	s_cselect_b64 s[6:7], -1, 0
	s_cmp_lg_u32 s9, 1
	s_cbranch_scc1 .LBB0_840
	s_barrier

.LBB0_856:
	v_readlane_b32 s4, v255, 36
	v_readlane_b32 s8, v252, 0
	s_add_i32 s5, s4, 10
	v_readlane_b32 s9, v252, 1
	s_cmp_ge_i32 s5, s9
	v_readlane_b32 s10, v252, 2
	v_readlane_b32 s11, v252, 3
	s_cbranch_scc1 .LBB0_906
	v_readlane_b32 s8, v252, 0
	v_readlane_b32 s9, v252, 1
	v_readlane_b32 s10, v252, 2
	v_readlane_b32 s11, v252, 3
